# s22 + fp8 GEMM unit loops (P8, P9): accumulators no longer zeroed with 128 v_mov per unit, the first K-tile's MFMAs take srcC = 0 (out-of-line copies of the first two MFMA blocks)
# baseline (speedup 1.0000x reference)
; #define PG8_BAR __builtin_amdgcn_s_barrier()
;     ...
; #pragma unroll
;         for (int a = 0; a < 2; ++a)
; #pragma unroll
;             for (int b = 0; b < 2; ++b)
; #pragma unroll
;                 for (int m = 0; m < 4; ++m)
; #pragma unroll
;                     for (int n = 0; n < 2; ++n) acc[a][b][m][n] = (f32x4){0.f, 0.f, 0.f, 0.f};
;         cur = nxt; cB = nB; ++ui;
;         if (wr == 1) PG8_BAR;
.LBB0_1033:
	s_add_u32 s43, s48, 0x100
	v_mov_b32_e32 v209, v201
	v_mov_b32_e32 v211, v201
	s_addc_u32 s45, s49, 0
	s_mov_b32 s70, -2
	s_mov_b64 s[48:49], s[28:29]
	s_branch .LBB0_1036
.Lmy_z80:
	v_mfma_scale_f32_16x16x128_f8f6f4 v[190:193], v[18:25], v[58:65], 0, v227, v226 op_sel_hi:[0,0,0]
	v_mfma_scale_f32_16x16x128_f8f6f4 v[182:185], v[26:33], v[58:65], 0, v227, v226 op_sel_hi:[0,0,0]
	v_mfma_scale_f32_16x16x128_f8f6f4 v[174:177], v[18:25], v[50:57], 0, v227, v226 op_sel_hi:[0,0,0]
	v_mfma_scale_f32_16x16x128_f8f6f4 v[166:169], v[26:33], v[50:57], 0, v227, v226 op_sel_hi:[0,0,0]
	v_mfma_scale_f32_16x16x128_f8f6f4 v[158:161], v[18:25], v[42:49], 0, v227, v226 op_sel_hi:[0,0,0]
	v_mfma_scale_f32_16x16x128_f8f6f4 v[150:153], v[26:33], v[42:49], 0, v227, v226 op_sel_hi:[0,0,0]
	v_mfma_scale_f32_16x16x128_f8f6f4 v[142:145], v[18:25], v[34:41], 0, v227, v226 op_sel_hi:[0,0,0]
	v_mfma_scale_f32_16x16x128_f8f6f4 v[134:137], v[26:33], v[34:41], 0, v227, v226 op_sel_hi:[0,0,0]
	s_setprio 0
	s_setprio 1
	v_mfma_scale_f32_16x16x128_f8f6f4 v[186:189], v[2:9], v[58:65], 0, v227, v226 op_sel_hi:[0,0,0]
	v_mfma_scale_f32_16x16x128_f8f6f4 v[178:181], v[10:17], v[58:65], 0, v227, v226 op_sel_hi:[0,0,0]
	v_mfma_scale_f32_16x16x128_f8f6f4 v[170:173], v[2:9], v[50:57], 0, v227, v226 op_sel_hi:[0,0,0]
	v_mfma_scale_f32_16x16x128_f8f6f4 v[162:165], v[10:17], v[50:57], 0, v227, v226 op_sel_hi:[0,0,0]
	v_mfma_scale_f32_16x16x128_f8f6f4 v[154:157], v[2:9], v[42:49], 0, v227, v226 op_sel_hi:[0,0,0]
	v_mfma_scale_f32_16x16x128_f8f6f4 v[146:149], v[10:17], v[42:49], 0, v227, v226 op_sel_hi:[0,0,0]
	v_mfma_scale_f32_16x16x128_f8f6f4 v[138:141], v[2:9], v[34:41], 0, v227, v226 op_sel_hi:[0,0,0]
	v_mfma_scale_f32_16x16x128_f8f6f4 v[130:133], v[10:17], v[34:41], 0, v227, v226 op_sel_hi:[0,0,0]
	s_branch .Lmy_z80_back
.Lmy_z81:
	v_mfma_scale_f32_16x16x128_f8f6f4 v[126:129], v[18:25], v[34:41], 0, v227, v226 op_sel_hi:[0,0,0]
	v_mfma_scale_f32_16x16x128_f8f6f4 v[118:121], v[26:33], v[34:41], 0, v227, v226 op_sel_hi:[0,0,0]
	v_mfma_scale_f32_16x16x128_f8f6f4 v[110:113], v[18:25], v[42:49], 0, v227, v226 op_sel_hi:[0,0,0]
	v_mfma_scale_f32_16x16x128_f8f6f4 v[102:105], v[26:33], v[42:49], 0, v227, v226 op_sel_hi:[0,0,0]
	v_mfma_scale_f32_16x16x128_f8f6f4 v[94:97], v[18:25], v[50:57], 0, v227, v226 op_sel_hi:[0,0,0]
	v_mfma_scale_f32_16x16x128_f8f6f4 v[86:89], v[26:33], v[50:57], 0, v227, v226 op_sel_hi:[0,0,0]
	v_mfma_scale_f32_16x16x128_f8f6f4 v[78:81], v[18:25], v[58:65], 0, v227, v226 op_sel_hi:[0,0,0]
	v_mfma_scale_f32_16x16x128_f8f6f4 v[70:73], v[26:33], v[58:65], 0, v227, v226 op_sel_hi:[0,0,0]
	s_setprio 0
	s_setprio 1
	v_mfma_scale_f32_16x16x128_f8f6f4 v[122:125], v[2:9], v[34:41], 0, v227, v226 op_sel_hi:[0,0,0]
	v_mfma_scale_f32_16x16x128_f8f6f4 v[114:117], v[10:17], v[34:41], 0, v227, v226 op_sel_hi:[0,0,0]
	v_mfma_scale_f32_16x16x128_f8f6f4 v[106:109], v[2:9], v[42:49], 0, v227, v226 op_sel_hi:[0,0,0]
	v_mfma_scale_f32_16x16x128_f8f6f4 v[98:101], v[10:17], v[42:49], 0, v227, v226 op_sel_hi:[0,0,0]
	v_mfma_scale_f32_16x16x128_f8f6f4 v[90:93], v[2:9], v[50:57], 0, v227, v226 op_sel_hi:[0,0,0]
	v_mfma_scale_f32_16x16x128_f8f6f4 v[82:85], v[10:17], v[50:57], 0, v227, v226 op_sel_hi:[0,0,0]
	v_mfma_scale_f32_16x16x128_f8f6f4 v[74:77], v[2:9], v[58:65], 0, v227, v226 op_sel_hi:[0,0,0]
	v_mfma_scale_f32_16x16x128_f8f6f4 v[66:69], v[10:17], v[58:65], 0, v227, v226 op_sel_hi:[0,0,0]
	s_branch .Lmy_z81_back

; #define PG8_STAGE(bufoff, gbase, voff) do { _Pragma("unroll") for (int _i = 0; _i < 2; ++_i) \
;         __builtin_amdgcn_global_load_lds((const unsigned*)((const char*)(gbase) + (voff)[_i]), (LAS unsigned*)(lds + (bufoff) + ldsw + _i * 8192), 16, 0, 0); } while (0)
; #define PG8_LDA(dst, b, h) do { _Pragma("unroll") for (int m = 0; m < 4; ++m) _Pragma("unroll") for (int k = 0; k < 2; ++k) dst[m][k] = *(const LAS bf16x8*)(lds + PG8_SA(b, h) + aoff + m * 2048 + k * 1024); } while (0)
; #define PG8_LDB(dst, b, h) do { _Pragma("unroll") for (int n = 0; n < 2; ++n) _Pragma("unroll") for (int k = 0; k < 2; ++k) dst[n][k] = *(const LAS bf16x8*)(lds + PG8_SB(b, h) + boff + n * 2048 + k * 1024); } while (0)
; #define PG8_WAIT_V(n) asm volatile("s_waitcnt vmcnt(" #n ")" ::: "memory")
; #define PG8_WAIT_L(n) asm volatile("s_waitcnt lgkmcnt(" #n ")" ::: "memory")
; #define PG8_BAR __builtin_amdgcn_s_barrier()
; #define PG8_SCHED __builtin_amdgcn_sched_barrier(0)
;     ...
;             const bool last = (t == nt - 2);
;             const char* a1 = cA + (size_t)(t + 1) * kstep;
;             const char* a2 = last ? cA : cA + (size_t)(t + 2) * kstep; const char* b2 = last ? nB : cB + (size_t)(t + 2) * kstep;
;             const char* a3 = a2 + kstep; const char* b3 = b2 + kstep;
;             PG8_LDB(B0, 0, 0); PG8_LDB(B1, 0, 1); PG8_SCHED; PG8_LDA(At, 0, 0); PG8_STAGE(PG8_SA(1, 1), a1, va[1]);
;             if (last) {
; #pragma unroll
;                 for (int h = 0; h < 2; ++h)
; #pragma unroll
;                     for (int i = 0; i < 2; ++i) va[h][i] = vn[h][i]; }
;             PG8_WAIT_V(8); PG8_WAIT_L(0); PG8_BAR; PG8_MMA(0, 0, At, B0); PG8_MMA(0, 1, At, B1); PG8_BAR; PG8_SCHED;
;             PG8_LDA(At, 0, 1); PG8_STAGE(PG8_SB(0, 0), b2, voffB); PG8_STAGE(PG8_SB(0, 1), b2 + hstep, voffB); PG8_STAGE(PG8_SA(0, 0), a2, va[0]);
;             PG8_WAIT_V(8); PG8_WAIT_L(0); PG8_BAR; PG8_MMA(1, 0, At, B0); PG8_MMA(1, 1, At, B1); PG8_BAR; PG8_SCHED;
.LBB0_1035:
	s_waitcnt vmcnt(8)
	s_add_u32 s54, s48, 0x80
	s_waitcnt lgkmcnt(0)
	s_addc_u32 s55, s49, 0
	s_and_b64 s[52:53], s[52:53], exec
	s_cselect_b32 s55, s27, s55
	s_cselect_b32 s54, s26, s54
	s_cselect_b32 s53, s47, s45
	s_cselect_b32 s52, s46, s43
	s_barrier
	s_setprio 1
	s_waitcnt lgkmcnt(0)
	s_cmpk_eq_i32 s70, -2
	s_cbranch_scc1 .Lmy_z80
	v_mfma_scale_f32_16x16x128_f8f6f4 v[190:193], v[18:25], v[58:65], v[190:193], v227, v226 op_sel_hi:[0,0,0]
	v_mfma_scale_f32_16x16x128_f8f6f4 v[182:185], v[26:33], v[58:65], v[182:185], v227, v226 op_sel_hi:[0,0,0]
	v_mfma_scale_f32_16x16x128_f8f6f4 v[174:177], v[18:25], v[50:57], v[174:177], v227, v226 op_sel_hi:[0,0,0]
	v_mfma_scale_f32_16x16x128_f8f6f4 v[166:169], v[26:33], v[50:57], v[166:169], v227, v226 op_sel_hi:[0,0,0]
	v_mfma_scale_f32_16x16x128_f8f6f4 v[158:161], v[18:25], v[42:49], v[158:161], v227, v226 op_sel_hi:[0,0,0]
	v_mfma_scale_f32_16x16x128_f8f6f4 v[150:153], v[26:33], v[42:49], v[150:153], v227, v226 op_sel_hi:[0,0,0]
	v_mfma_scale_f32_16x16x128_f8f6f4 v[142:145], v[18:25], v[34:41], v[142:145], v227, v226 op_sel_hi:[0,0,0]
	v_mfma_scale_f32_16x16x128_f8f6f4 v[134:137], v[26:33], v[34:41], v[134:137], v227, v226 op_sel_hi:[0,0,0]
	s_setprio 0
	s_setprio 1
	v_mfma_scale_f32_16x16x128_f8f6f4 v[186:189], v[2:9], v[58:65], v[186:189], v227, v226 op_sel_hi:[0,0,0]
	v_mfma_scale_f32_16x16x128_f8f6f4 v[178:181], v[10:17], v[58:65], v[178:181], v227, v226 op_sel_hi:[0,0,0]
	v_mfma_scale_f32_16x16x128_f8f6f4 v[170:173], v[2:9], v[50:57], v[170:173], v227, v226 op_sel_hi:[0,0,0]
	v_mfma_scale_f32_16x16x128_f8f6f4 v[162:165], v[10:17], v[50:57], v[162:165], v227, v226 op_sel_hi:[0,0,0]
	v_mfma_scale_f32_16x16x128_f8f6f4 v[154:157], v[2:9], v[42:49], v[154:157], v227, v226 op_sel_hi:[0,0,0]
	v_mfma_scale_f32_16x16x128_f8f6f4 v[146:149], v[10:17], v[42:49], v[146:149], v227, v226 op_sel_hi:[0,0,0]
	v_mfma_scale_f32_16x16x128_f8f6f4 v[138:141], v[2:9], v[34:41], v[138:141], v227, v226 op_sel_hi:[0,0,0]
	v_mfma_scale_f32_16x16x128_f8f6f4 v[130:133], v[10:17], v[34:41], v[130:133], v227, v226 op_sel_hi:[0,0,0]
.Lmy_z80_back:
	s_setprio 0
	s_barrier
	s_mov_b32 m0, s37
	v_lshl_add_u64 v[232:233], s[52:53], 0, v[196:197]
	s_add_u32 s72, s52, 0x40000
	ds_read_b128 v[34:37], v225 offset:16384
	ds_read_b128 v[38:41], v225 offset:17408
	ds_read_b128 v[42:45], v225 offset:18432
	ds_read_b128 v[46:49], v225 offset:19456
	ds_read_b128 v[50:53], v225 offset:20480
	ds_read_b128 v[54:57], v225 offset:21504
	ds_read_b128 v[58:61], v225 offset:22528
	ds_read_b128 v[62:65], v225 offset:23552
	global_load_lds_dwordx4 v[232:233], off
	v_lshl_add_u64 v[234:235], s[52:53], 0, v[198:199]
	s_mov_b32 m0, s39
	s_addc_u32 s73, s53, 0
	global_load_lds_dwordx4 v[234:235], off
	v_lshl_add_u64 v[236:237], s[72:73], 0, v[196:197]
	s_mov_b32 m0, s41
	v_mov_b32_e32 v205, v201
	global_load_lds_dwordx4 v[236:237], off
	v_lshl_add_u64 v[236:237], s[72:73], 0, v[198:199]
	s_mov_b32 m0, s56
	v_lshl_add_u64 v[238:239], s[54:55], 0, v[204:205]
	global_load_lds_dwordx4 v[236:237], off
	s_mov_b32 m0, s35
	v_lshl_add_u64 v[236:237], s[54:55], 0, v[200:201]
	global_load_lds_dwordx4 v200, s[54:55]
	s_mov_b32 m0, s57
	s_nop 0
	global_load_lds_dwordx4 v204, s[54:55]
	s_waitcnt vmcnt(8)
	s_waitcnt lgkmcnt(0)
	s_barrier
	s_setprio 1
	s_waitcnt lgkmcnt(0)
	s_cmpk_eq_i32 s70, -2
	s_cbranch_scc1 .Lmy_z81
	v_mfma_scale_f32_16x16x128_f8f6f4 v[126:129], v[18:25], v[34:41], v[126:129], v227, v226 op_sel_hi:[0,0,0]
	v_mfma_scale_f32_16x16x128_f8f6f4 v[118:121], v[26:33], v[34:41], v[118:121], v227, v226 op_sel_hi:[0,0,0]
	v_mfma_scale_f32_16x16x128_f8f6f4 v[110:113], v[18:25], v[42:49], v[110:113], v227, v226 op_sel_hi:[0,0,0]
	v_mfma_scale_f32_16x16x128_f8f6f4 v[102:105], v[26:33], v[42:49], v[102:105], v227, v226 op_sel_hi:[0,0,0]
	v_mfma_scale_f32_16x16x128_f8f6f4 v[94:97], v[18:25], v[50:57], v[94:97], v227, v226 op_sel_hi:[0,0,0]
	v_mfma_scale_f32_16x16x128_f8f6f4 v[86:89], v[26:33], v[50:57], v[86:89], v227, v226 op_sel_hi:[0,0,0]
	v_mfma_scale_f32_16x16x128_f8f6f4 v[78:81], v[18:25], v[58:65], v[78:81], v227, v226 op_sel_hi:[0,0,0]
	v_mfma_scale_f32_16x16x128_f8f6f4 v[70:73], v[26:33], v[58:65], v[70:73], v227, v226 op_sel_hi:[0,0,0]
	s_setprio 0
	s_setprio 1
	v_mfma_scale_f32_16x16x128_f8f6f4 v[122:125], v[2:9], v[34:41], v[122:125], v227, v226 op_sel_hi:[0,0,0]
	v_mfma_scale_f32_16x16x128_f8f6f4 v[114:117], v[10:17], v[34:41], v[114:117], v227, v226 op_sel_hi:[0,0,0]
	v_mfma_scale_f32_16x16x128_f8f6f4 v[106:109], v[2:9], v[42:49], v[106:109], v227, v226 op_sel_hi:[0,0,0]
	v_mfma_scale_f32_16x16x128_f8f6f4 v[98:101], v[10:17], v[42:49], v[98:101], v227, v226 op_sel_hi:[0,0,0]
	v_mfma_scale_f32_16x16x128_f8f6f4 v[90:93], v[2:9], v[50:57], v[90:93], v227, v226 op_sel_hi:[0,0,0]
	v_mfma_scale_f32_16x16x128_f8f6f4 v[82:85], v[10:17], v[50:57], v[82:85], v227, v226 op_sel_hi:[0,0,0]
	v_mfma_scale_f32_16x16x128_f8f6f4 v[74:77], v[2:9], v[58:65], v[74:77], v227, v226 op_sel_hi:[0,0,0]
	v_mfma_scale_f32_16x16x128_f8f6f4 v[66:69], v[10:17], v[58:65], v[66:69], v227, v226 op_sel_hi:[0,0,0]
; #define PG8_STAGE(bufoff, gbase, voff) do { _Pragma("unroll") for (int _i = 0; _i < 2; ++_i) \
;         __builtin_amdgcn_global_load_lds((const unsigned*)((const char*)(gbase) + (voff)[_i]), (LAS unsigned*)(lds + (bufoff) + ldsw + _i * 8192), 16, 0, 0); } while (0)
; #define PG8_LDA(dst, b, h) do { _Pragma("unroll") for (int m = 0; m < 4; ++m) _Pragma("unroll") for (int k = 0; k < 2; ++k) dst[m][k] = *(const LAS bf16x8*)(lds + PG8_SA(b, h) + aoff + m * 2048 + k * 1024); } while (0)
; #define PG8_LDB(dst, b, h) do { _Pragma("unroll") for (int n = 0; n < 2; ++n) _Pragma("unroll") for (int k = 0; k < 2; ++k) dst[n][k] = *(const LAS bf16x8*)(lds + PG8_SB(b, h) + boff + n * 2048 + k * 1024); } while (0)
; #define PG8_WAIT_V(n) asm volatile("s_waitcnt vmcnt(" #n ")" ::: "memory")
; #define PG8_WAIT_L(n) asm volatile("s_waitcnt lgkmcnt(" #n ")" ::: "memory")
; #define PG8_BAR __builtin_amdgcn_s_barrier()
; #define PG8_SCHED __builtin_amdgcn_sched_barrier(0)
;     ...
;             PG8_LDB(B0, 1, 0); PG8_LDB(B1, 1, 1); PG8_SCHED; PG8_LDA(At, 1, 0); PG8_STAGE(PG8_SA(0, 1), a2, va[1]);
;             PG8_WAIT_V(8); PG8_WAIT_L(0); PG8_BAR; PG8_MMA(0, 0, At, B0); PG8_MMA(0, 1, At, B1); PG8_BAR; PG8_SCHED;
;             PG8_LDA(At, 1, 1); PG8_STAGE(PG8_SB(1, 0), b3, voffB); PG8_STAGE(PG8_SB(1, 1), b3 + hstep, voffB); PG8_STAGE(PG8_SA(1, 0), a3, va[0]);
;             PG8_WAIT_V(8); PG8_WAIT_L(0); PG8_BAR; PG8_MMA(1, 0, At, B0); PG8_MMA(1, 1, At, B1); PG8_BAR; PG8_SCHED;
;         }
.Lmy_z81_back:
	s_setprio 0
	s_barrier
	s_add_i32 s71, 0, 0x18000
	s_add_i32 s72, 0, 0x1c000
	v_add_u32_e32 v14, s71, v219
	v_add_u32_e32 v30, s72, v219
	ds_read_b128 v[2:5], v14
	ds_read_b128 v[6:9], v14 offset:1024
	ds_read_b128 v[10:13], v14 offset:2048
	ds_read_b128 v[14:17], v14 offset:3072
	ds_read_b128 v[18:21], v30
	ds_read_b128 v[22:25], v30 offset:1024
	ds_read_b128 v[26:29], v30 offset:2048
	ds_read_b128 v[30:33], v30 offset:3072
	s_mov_b32 m0, s59
	v_lshl_add_u64 v[214:215], s[54:55], 0, v[214:215]
	ds_read_b128 v[34:37], v225 offset:32768
	ds_read_b128 v[38:41], v225 offset:33792
	ds_read_b128 v[42:45], v225 offset:34816
	ds_read_b128 v[46:49], v225 offset:35840
	ds_read_b128 v[50:53], v225 offset:36864
	ds_read_b128 v[54:57], v225 offset:37888
	ds_read_b128 v[58:61], v225 offset:38912
	ds_read_b128 v[62:65], v225 offset:39936
	global_load_lds_dwordx4 v[214:215], off
	v_lshl_add_u64 v[212:213], s[54:55], 0, v[212:213]
	s_mov_b32 m0, s60
	s_nop 0
	global_load_lds_dwordx4 v[212:213], off
	s_waitcnt vmcnt(8)
	s_waitcnt lgkmcnt(0)
	s_barrier
	s_setprio 1
	s_waitcnt lgkmcnt(0)
	v_mfma_scale_f32_16x16x128_f8f6f4 v[190:193], v[2:9], v[34:41], v[190:193], v227, v226 op_sel_hi:[0,0,0]
	v_mfma_scale_f32_16x16x128_f8f6f4 v[182:185], v[10:17], v[34:41], v[182:185], v227, v226 op_sel_hi:[0,0,0]
	v_mfma_scale_f32_16x16x128_f8f6f4 v[174:177], v[2:9], v[42:49], v[174:177], v227, v226 op_sel_hi:[0,0,0]
	v_mfma_scale_f32_16x16x128_f8f6f4 v[166:169], v[10:17], v[42:49], v[166:169], v227, v226 op_sel_hi:[0,0,0]
	v_mfma_scale_f32_16x16x128_f8f6f4 v[158:161], v[2:9], v[50:57], v[158:161], v227, v226 op_sel_hi:[0,0,0]
	v_mfma_scale_f32_16x16x128_f8f6f4 v[150:153], v[10:17], v[50:57], v[150:153], v227, v226 op_sel_hi:[0,0,0]
	v_mfma_scale_f32_16x16x128_f8f6f4 v[142:145], v[2:9], v[58:65], v[142:145], v227, v226 op_sel_hi:[0,0,0]
	v_mfma_scale_f32_16x16x128_f8f6f4 v[134:137], v[10:17], v[58:65], v[134:137], v227, v226 op_sel_hi:[0,0,0]
	s_setprio 0
	s_setprio 1
	v_mfma_scale_f32_16x16x128_f8f6f4 v[186:189], v[18:25], v[34:41], v[186:189], v227, v226 op_sel_hi:[0,0,0]
	v_mfma_scale_f32_16x16x128_f8f6f4 v[178:181], v[26:33], v[34:41], v[178:181], v227, v226 op_sel_hi:[0,0,0]
	v_mfma_scale_f32_16x16x128_f8f6f4 v[170:173], v[18:25], v[42:49], v[170:173], v227, v226 op_sel_hi:[0,0,0]
	v_mfma_scale_f32_16x16x128_f8f6f4 v[162:165], v[26:33], v[42:49], v[162:165], v227, v226 op_sel_hi:[0,0,0]
	v_mfma_scale_f32_16x16x128_f8f6f4 v[154:157], v[18:25], v[50:57], v[154:157], v227, v226 op_sel_hi:[0,0,0]
	v_mfma_scale_f32_16x16x128_f8f6f4 v[146:149], v[26:33], v[50:57], v[146:149], v227, v226 op_sel_hi:[0,0,0]
	v_mfma_scale_f32_16x16x128_f8f6f4 v[138:141], v[18:25], v[58:65], v[138:141], v227, v226 op_sel_hi:[0,0,0]
	v_mfma_scale_f32_16x16x128_f8f6f4 v[130:133], v[26:33], v[58:65], v[130:133], v227, v226 op_sel_hi:[0,0,0]
	s_setprio 0
	s_barrier
	s_add_i32 s54, s71, s2
	v_lshl_add_u64 v[212:213], v[232:233], 0, s[14:15]
	s_mov_b32 m0, s54
	ds_read_b128 v[34:37], v225 offset:49152
	ds_read_b128 v[38:41], v225 offset:50176
	ds_read_b128 v[42:45], v225 offset:51200
	ds_read_b128 v[46:49], v225 offset:52224
	ds_read_b128 v[50:53], v225 offset:53248
	ds_read_b128 v[54:57], v225 offset:54272
	ds_read_b128 v[58:61], v225 offset:55296
	ds_read_b128 v[62:65], v225 offset:56320
	global_load_lds_dwordx4 v[212:213], off
	s_add_i32 m0, s54, 0x2000
	s_add_u32 s52, s52, 0x40080
	v_lshl_add_u64 v[212:213], v[234:235], 0, s[14:15]
	s_addc_u32 s53, s53, 0
	s_add_i32 s54, s72, s2
	global_load_lds_dwordx4 v[212:213], off
	v_lshl_add_u64 v[212:213], s[52:53], 0, v[196:197]
	s_mov_b32 m0, s54
	s_nop 0
	global_load_lds_dwordx4 v[212:213], off
	v_lshl_add_u64 v[212:213], s[52:53], 0, v[198:199]
	s_add_i32 m0, s54, 0x2000
	s_nop 0
	global_load_lds_dwordx4 v[212:213], off
	v_lshl_add_u64 v[212:213], v[236:237], 0, s[14:15]
	s_mov_b32 m0, s62
	s_nop 0
	global_load_lds_dwordx4 v[212:213], off
	v_lshl_add_u64 v[212:213], v[238:239], 0, s[14:15]
	s_mov_b32 m0, s63
	s_nop 0
	global_load_lds_dwordx4 v[212:213], off
	s_waitcnt vmcnt(8)
	s_waitcnt lgkmcnt(0)
	s_barrier
	s_setprio 1
	s_waitcnt lgkmcnt(0)
	v_mfma_scale_f32_16x16x128_f8f6f4 v[126:129], v[2:9], v[34:41], v[126:129], v227, v226 op_sel_hi:[0,0,0]
	v_mfma_scale_f32_16x16x128_f8f6f4 v[118:121], v[10:17], v[34:41], v[118:121], v227, v226 op_sel_hi:[0,0,0]
	v_mfma_scale_f32_16x16x128_f8f6f4 v[110:113], v[2:9], v[42:49], v[110:113], v227, v226 op_sel_hi:[0,0,0]
	v_mfma_scale_f32_16x16x128_f8f6f4 v[102:105], v[10:17], v[42:49], v[102:105], v227, v226 op_sel_hi:[0,0,0]
	v_mfma_scale_f32_16x16x128_f8f6f4 v[94:97], v[2:9], v[50:57], v[94:97], v227, v226 op_sel_hi:[0,0,0]
	v_mfma_scale_f32_16x16x128_f8f6f4 v[86:89], v[10:17], v[50:57], v[86:89], v227, v226 op_sel_hi:[0,0,0]
	v_mfma_scale_f32_16x16x128_f8f6f4 v[78:81], v[2:9], v[58:65], v[78:81], v227, v226 op_sel_hi:[0,0,0]
	v_mfma_scale_f32_16x16x128_f8f6f4 v[70:73], v[10:17], v[58:65], v[70:73], v227, v226 op_sel_hi:[0,0,0]
	s_setprio 0
	s_setprio 1
	v_mfma_scale_f32_16x16x128_f8f6f4 v[122:125], v[18:25], v[34:41], v[122:125], v227, v226 op_sel_hi:[0,0,0]
	v_mfma_scale_f32_16x16x128_f8f6f4 v[114:117], v[26:33], v[34:41], v[114:117], v227, v226 op_sel_hi:[0,0,0]
	v_mfma_scale_f32_16x16x128_f8f6f4 v[106:109], v[18:25], v[42:49], v[106:109], v227, v226 op_sel_hi:[0,0,0]
	v_mfma_scale_f32_16x16x128_f8f6f4 v[98:101], v[26:33], v[42:49], v[98:101], v227, v226 op_sel_hi:[0,0,0]
	v_mfma_scale_f32_16x16x128_f8f6f4 v[90:93], v[18:25], v[50:57], v[90:93], v227, v226 op_sel_hi:[0,0,0]
	v_mfma_scale_f32_16x16x128_f8f6f4 v[82:85], v[26:33], v[50:57], v[82:85], v227, v226 op_sel_hi:[0,0,0]
	v_mfma_scale_f32_16x16x128_f8f6f4 v[74:77], v[18:25], v[58:65], v[74:77], v227, v226 op_sel_hi:[0,0,0]
	v_mfma_scale_f32_16x16x128_f8f6f4 v[66:69], v[26:33], v[58:65], v[66:69], v227, v226 op_sel_hi:[0,0,0]
	s_setprio 0
	s_barrier
	s_add_i32 s70, s70, 2
	s_add_u32 s43, s43, 0x100
	s_addc_u32 s45, s45, 0
	s_add_u32 s48, s48, 0x100
	s_addc_u32 s49, s49, 0
	s_cmp_gt_u32 s70, 13
	s_cbranch_scc1 .LBB0_1038

; #define PG8_BAR __builtin_amdgcn_s_barrier()
;     ...
; #pragma unroll
;         for (int a = 0; a < 2; ++a)
; #pragma unroll
;             for (int b = 0; b < 2; ++b)
; #pragma unroll
;                 for (int m = 0; m < 4; ++m)
; #pragma unroll
;                     for (int n = 0; n < 2; ++n) acc[a][b][m][n] = (f32x4){0.f, 0.f, 0.f, 0.f};
;         cur = nxt; cB = nB; ++ui;
;         if (wr == 1) PG8_BAR;
.LBB0_1185:
	s_add_u32 s27, s34, 0x100
	v_mov_b32_e32 v209, v201
	v_mov_b32_e32 v211, v201
	s_addc_u32 s29, s35, 0
	s_mov_b32 s62, -2
	s_mov_b64 s[34:35], s[12:13]
	s_branch .LBB0_1188
.Lmy_z90:
	v_mfma_scale_f32_16x16x128_f8f6f4 v[190:193], v[18:25], v[58:65], 0, v227, v226 op_sel_hi:[0,0,0]
	v_mfma_scale_f32_16x16x128_f8f6f4 v[186:189], v[26:33], v[58:65], 0, v227, v226 op_sel_hi:[0,0,0]
	v_mfma_scale_f32_16x16x128_f8f6f4 v[182:185], v[18:25], v[50:57], 0, v227, v226 op_sel_hi:[0,0,0]
	v_mfma_scale_f32_16x16x128_f8f6f4 v[178:181], v[26:33], v[50:57], 0, v227, v226 op_sel_hi:[0,0,0]
	v_mfma_scale_f32_16x16x128_f8f6f4 v[158:161], v[18:25], v[42:49], 0, v227, v226 op_sel_hi:[0,0,0]
	v_mfma_scale_f32_16x16x128_f8f6f4 v[154:157], v[26:33], v[42:49], 0, v227, v226 op_sel_hi:[0,0,0]
	v_mfma_scale_f32_16x16x128_f8f6f4 v[150:153], v[18:25], v[34:41], 0, v227, v226 op_sel_hi:[0,0,0]
	v_mfma_scale_f32_16x16x128_f8f6f4 v[146:149], v[26:33], v[34:41], 0, v227, v226 op_sel_hi:[0,0,0]
	s_setprio 0
	s_setprio 1
	v_mfma_scale_f32_16x16x128_f8f6f4 v[174:177], v[2:9], v[58:65], 0, v227, v226 op_sel_hi:[0,0,0]
	v_mfma_scale_f32_16x16x128_f8f6f4 v[170:173], v[10:17], v[58:65], 0, v227, v226 op_sel_hi:[0,0,0]
	v_mfma_scale_f32_16x16x128_f8f6f4 v[166:169], v[2:9], v[50:57], 0, v227, v226 op_sel_hi:[0,0,0]
	v_mfma_scale_f32_16x16x128_f8f6f4 v[162:165], v[10:17], v[50:57], 0, v227, v226 op_sel_hi:[0,0,0]
	v_mfma_scale_f32_16x16x128_f8f6f4 v[142:145], v[2:9], v[42:49], 0, v227, v226 op_sel_hi:[0,0,0]
	v_mfma_scale_f32_16x16x128_f8f6f4 v[138:141], v[10:17], v[42:49], 0, v227, v226 op_sel_hi:[0,0,0]
	v_mfma_scale_f32_16x16x128_f8f6f4 v[134:137], v[2:9], v[34:41], 0, v227, v226 op_sel_hi:[0,0,0]
	v_mfma_scale_f32_16x16x128_f8f6f4 v[130:133], v[10:17], v[34:41], 0, v227, v226 op_sel_hi:[0,0,0]
	s_branch .Lmy_z90_back
.Lmy_z91:
	v_mfma_scale_f32_16x16x128_f8f6f4 v[126:129], v[18:25], v[34:41], 0, v227, v226 op_sel_hi:[0,0,0]
	v_mfma_scale_f32_16x16x128_f8f6f4 v[122:125], v[26:33], v[34:41], 0, v227, v226 op_sel_hi:[0,0,0]
	v_mfma_scale_f32_16x16x128_f8f6f4 v[118:121], v[18:25], v[42:49], 0, v227, v226 op_sel_hi:[0,0,0]
	v_mfma_scale_f32_16x16x128_f8f6f4 v[114:117], v[26:33], v[42:49], 0, v227, v226 op_sel_hi:[0,0,0]
	v_mfma_scale_f32_16x16x128_f8f6f4 v[94:97], v[18:25], v[50:57], 0, v227, v226 op_sel_hi:[0,0,0]
	v_mfma_scale_f32_16x16x128_f8f6f4 v[90:93], v[26:33], v[50:57], 0, v227, v226 op_sel_hi:[0,0,0]
	v_mfma_scale_f32_16x16x128_f8f6f4 v[86:89], v[18:25], v[58:65], 0, v227, v226 op_sel_hi:[0,0,0]
	v_mfma_scale_f32_16x16x128_f8f6f4 v[82:85], v[26:33], v[58:65], 0, v227, v226 op_sel_hi:[0,0,0]
	s_setprio 0
	s_setprio 1
	v_mfma_scale_f32_16x16x128_f8f6f4 v[110:113], v[2:9], v[34:41], 0, v227, v226 op_sel_hi:[0,0,0]
	v_mfma_scale_f32_16x16x128_f8f6f4 v[106:109], v[10:17], v[34:41], 0, v227, v226 op_sel_hi:[0,0,0]
	v_mfma_scale_f32_16x16x128_f8f6f4 v[102:105], v[2:9], v[42:49], 0, v227, v226 op_sel_hi:[0,0,0]
	v_mfma_scale_f32_16x16x128_f8f6f4 v[98:101], v[10:17], v[42:49], 0, v227, v226 op_sel_hi:[0,0,0]
	v_mfma_scale_f32_16x16x128_f8f6f4 v[78:81], v[2:9], v[50:57], 0, v227, v226 op_sel_hi:[0,0,0]
	v_mfma_scale_f32_16x16x128_f8f6f4 v[74:77], v[10:17], v[50:57], 0, v227, v226 op_sel_hi:[0,0,0]
	v_mfma_scale_f32_16x16x128_f8f6f4 v[70:73], v[2:9], v[58:65], 0, v227, v226 op_sel_hi:[0,0,0]
	v_mfma_scale_f32_16x16x128_f8f6f4 v[66:69], v[10:17], v[58:65], 0, v227, v226 op_sel_hi:[0,0,0]
	s_branch .Lmy_z91_back

; #define PG8_STAGE(bufoff, gbase, voff) do { _Pragma("unroll") for (int _i = 0; _i < 2; ++_i) \
;         __builtin_amdgcn_global_load_lds((const unsigned*)((const char*)(gbase) + (voff)[_i]), (LAS unsigned*)(lds + (bufoff) + ldsw + _i * 8192), 16, 0, 0); } while (0)
; #define PG8_LDA(dst, b, h) do { _Pragma("unroll") for (int m = 0; m < 4; ++m) _Pragma("unroll") for (int k = 0; k < 2; ++k) dst[m][k] = *(const LAS bf16x8*)(lds + PG8_SA(b, h) + aoff + m * 2048 + k * 1024); } while (0)
; #define PG8_LDB(dst, b, h) do { _Pragma("unroll") for (int n = 0; n < 2; ++n) _Pragma("unroll") for (int k = 0; k < 2; ++k) dst[n][k] = *(const LAS bf16x8*)(lds + PG8_SB(b, h) + boff + n * 2048 + k * 1024); } while (0)
; #define PG8_WAIT_V(n) asm volatile("s_waitcnt vmcnt(" #n ")" ::: "memory")
; #define PG8_WAIT_L(n) asm volatile("s_waitcnt lgkmcnt(" #n ")" ::: "memory")
; #define PG8_BAR __builtin_amdgcn_s_barrier()
; #define PG8_SCHED __builtin_amdgcn_sched_barrier(0)
;     ...
;             const bool last = (t == nt - 2);
;             const char* a1 = cA + (size_t)(t + 1) * kstep;
;             const char* a2 = last ? cA : cA + (size_t)(t + 2) * kstep; const char* b2 = last ? nB : cB + (size_t)(t + 2) * kstep;
;             const char* a3 = a2 + kstep; const char* b3 = b2 + kstep;
;             PG8_LDB(B0, 0, 0); PG8_LDB(B1, 0, 1); PG8_SCHED; PG8_LDA(At, 0, 0); PG8_STAGE(PG8_SA(1, 1), a1, va[1]);
;             if (last) {
; #pragma unroll
;                 for (int h = 0; h < 2; ++h)
; #pragma unroll
;                     for (int i = 0; i < 2; ++i) va[h][i] = vn[h][i]; }
;             PG8_WAIT_V(8); PG8_WAIT_L(0); PG8_BAR; PG8_MMA(0, 0, At, B0); PG8_MMA(0, 1, At, B1); PG8_BAR; PG8_SCHED;
;             PG8_LDA(At, 0, 1); PG8_STAGE(PG8_SB(0, 0), b2, voffB); PG8_STAGE(PG8_SB(0, 1), b2 + hstep, voffB); PG8_STAGE(PG8_SA(0, 0), a2, va[0]);
;             PG8_WAIT_V(8); PG8_WAIT_L(0); PG8_BAR; PG8_MMA(1, 0, At, B0); PG8_MMA(1, 1, At, B1); PG8_BAR; PG8_SCHED;
.LBB0_1187:
	s_waitcnt vmcnt(8)
	s_add_u32 s38, s34, 0x80
	s_waitcnt lgkmcnt(0)
	s_addc_u32 s39, s35, 0
	s_and_b64 s[36:37], s[36:37], exec
	s_cselect_b32 s39, s17, s39
	s_cselect_b32 s38, s16, s38
	s_cselect_b32 s37, s31, s29
	s_cselect_b32 s36, s30, s27
	s_barrier
	s_setprio 1
	s_waitcnt lgkmcnt(0)
	s_cmpk_eq_i32 s62, -2
	s_cbranch_scc1 .Lmy_z90
	v_mfma_scale_f32_16x16x128_f8f6f4 v[190:193], v[18:25], v[58:65], v[190:193], v227, v226 op_sel_hi:[0,0,0]
	v_mfma_scale_f32_16x16x128_f8f6f4 v[186:189], v[26:33], v[58:65], v[186:189], v227, v226 op_sel_hi:[0,0,0]
	v_mfma_scale_f32_16x16x128_f8f6f4 v[182:185], v[18:25], v[50:57], v[182:185], v227, v226 op_sel_hi:[0,0,0]
	v_mfma_scale_f32_16x16x128_f8f6f4 v[178:181], v[26:33], v[50:57], v[178:181], v227, v226 op_sel_hi:[0,0,0]
	v_mfma_scale_f32_16x16x128_f8f6f4 v[158:161], v[18:25], v[42:49], v[158:161], v227, v226 op_sel_hi:[0,0,0]
	v_mfma_scale_f32_16x16x128_f8f6f4 v[154:157], v[26:33], v[42:49], v[154:157], v227, v226 op_sel_hi:[0,0,0]
	v_mfma_scale_f32_16x16x128_f8f6f4 v[150:153], v[18:25], v[34:41], v[150:153], v227, v226 op_sel_hi:[0,0,0]
	v_mfma_scale_f32_16x16x128_f8f6f4 v[146:149], v[26:33], v[34:41], v[146:149], v227, v226 op_sel_hi:[0,0,0]
	s_setprio 0
	s_setprio 1
	v_mfma_scale_f32_16x16x128_f8f6f4 v[174:177], v[2:9], v[58:65], v[174:177], v227, v226 op_sel_hi:[0,0,0]
	v_mfma_scale_f32_16x16x128_f8f6f4 v[170:173], v[10:17], v[58:65], v[170:173], v227, v226 op_sel_hi:[0,0,0]
	v_mfma_scale_f32_16x16x128_f8f6f4 v[166:169], v[2:9], v[50:57], v[166:169], v227, v226 op_sel_hi:[0,0,0]
	v_mfma_scale_f32_16x16x128_f8f6f4 v[162:165], v[10:17], v[50:57], v[162:165], v227, v226 op_sel_hi:[0,0,0]
	v_mfma_scale_f32_16x16x128_f8f6f4 v[142:145], v[2:9], v[42:49], v[142:145], v227, v226 op_sel_hi:[0,0,0]
	v_mfma_scale_f32_16x16x128_f8f6f4 v[138:141], v[10:17], v[42:49], v[138:141], v227, v226 op_sel_hi:[0,0,0]
	v_mfma_scale_f32_16x16x128_f8f6f4 v[134:137], v[2:9], v[34:41], v[134:137], v227, v226 op_sel_hi:[0,0,0]
	v_mfma_scale_f32_16x16x128_f8f6f4 v[130:133], v[10:17], v[34:41], v[130:133], v227, v226 op_sel_hi:[0,0,0]
.Lmy_z90_back:
	s_setprio 0
	s_barrier
	s_mov_b32 m0, s25
	v_lshl_add_u64 v[230:231], s[36:37], 0, v[198:199]
	s_add_u32 s64, s36, 0x40000
	ds_read_b128 v[34:37], v225 offset:16384
	ds_read_b128 v[38:41], v225 offset:17408
	ds_read_b128 v[42:45], v225 offset:18432
	ds_read_b128 v[46:49], v225 offset:19456
	ds_read_b128 v[50:53], v225 offset:20480
	ds_read_b128 v[54:57], v225 offset:21504
	ds_read_b128 v[58:61], v225 offset:22528
	ds_read_b128 v[62:65], v225 offset:23552
	global_load_lds_dwordx4 v[230:231], off
	v_lshl_add_u64 v[232:233], s[36:37], 0, v[196:197]
	s_mov_b32 m0, s33
	s_addc_u32 s65, s37, 0
	global_load_lds_dwordx4 v[232:233], off
	v_lshl_add_u64 v[234:235], s[64:65], 0, v[198:199]
	s_mov_b32 m0, s40
	v_mov_b32_e32 v207, v201
	global_load_lds_dwordx4 v[234:235], off
	v_lshl_add_u64 v[234:235], s[64:65], 0, v[196:197]
	s_mov_b32 m0, s41
	v_lshl_add_u64 v[236:237], s[38:39], 0, v[206:207]
	global_load_lds_dwordx4 v[234:235], off
	s_mov_b32 m0, s3
	v_lshl_add_u64 v[234:235], s[38:39], 0, v[200:201]
	global_load_lds_dwordx4 v200, s[38:39]
	s_mov_b32 m0, s42
	s_nop 0
	global_load_lds_dwordx4 v206, s[38:39]
	s_waitcnt vmcnt(8)
	s_waitcnt lgkmcnt(0)
	s_barrier
	s_setprio 1
	s_waitcnt lgkmcnt(0)
	s_cmpk_eq_i32 s62, -2
	s_cbranch_scc1 .Lmy_z91
	v_mfma_scale_f32_16x16x128_f8f6f4 v[126:129], v[18:25], v[34:41], v[126:129], v227, v226 op_sel_hi:[0,0,0]
	v_mfma_scale_f32_16x16x128_f8f6f4 v[122:125], v[26:33], v[34:41], v[122:125], v227, v226 op_sel_hi:[0,0,0]
	v_mfma_scale_f32_16x16x128_f8f6f4 v[118:121], v[18:25], v[42:49], v[118:121], v227, v226 op_sel_hi:[0,0,0]
	v_mfma_scale_f32_16x16x128_f8f6f4 v[114:117], v[26:33], v[42:49], v[114:117], v227, v226 op_sel_hi:[0,0,0]
	v_mfma_scale_f32_16x16x128_f8f6f4 v[94:97], v[18:25], v[50:57], v[94:97], v227, v226 op_sel_hi:[0,0,0]
	v_mfma_scale_f32_16x16x128_f8f6f4 v[90:93], v[26:33], v[50:57], v[90:93], v227, v226 op_sel_hi:[0,0,0]
	v_mfma_scale_f32_16x16x128_f8f6f4 v[86:89], v[18:25], v[58:65], v[86:89], v227, v226 op_sel_hi:[0,0,0]
	v_mfma_scale_f32_16x16x128_f8f6f4 v[82:85], v[26:33], v[58:65], v[82:85], v227, v226 op_sel_hi:[0,0,0]
	s_setprio 0
	s_setprio 1
	v_mfma_scale_f32_16x16x128_f8f6f4 v[110:113], v[2:9], v[34:41], v[110:113], v227, v226 op_sel_hi:[0,0,0]
	v_mfma_scale_f32_16x16x128_f8f6f4 v[106:109], v[10:17], v[34:41], v[106:109], v227, v226 op_sel_hi:[0,0,0]
	v_mfma_scale_f32_16x16x128_f8f6f4 v[102:105], v[2:9], v[42:49], v[102:105], v227, v226 op_sel_hi:[0,0,0]
	v_mfma_scale_f32_16x16x128_f8f6f4 v[98:101], v[10:17], v[42:49], v[98:101], v227, v226 op_sel_hi:[0,0,0]
	v_mfma_scale_f32_16x16x128_f8f6f4 v[78:81], v[2:9], v[50:57], v[78:81], v227, v226 op_sel_hi:[0,0,0]
	v_mfma_scale_f32_16x16x128_f8f6f4 v[74:77], v[10:17], v[50:57], v[74:77], v227, v226 op_sel_hi:[0,0,0]
	v_mfma_scale_f32_16x16x128_f8f6f4 v[70:73], v[2:9], v[58:65], v[70:73], v227, v226 op_sel_hi:[0,0,0]
	v_mfma_scale_f32_16x16x128_f8f6f4 v[66:69], v[10:17], v[58:65], v[66:69], v227, v226 op_sel_hi:[0,0,0]
; #define PG8_STAGE(bufoff, gbase, voff) do { _Pragma("unroll") for (int _i = 0; _i < 2; ++_i) \
;         __builtin_amdgcn_global_load_lds((const unsigned*)((const char*)(gbase) + (voff)[_i]), (LAS unsigned*)(lds + (bufoff) + ldsw + _i * 8192), 16, 0, 0); } while (0)
; #define PG8_LDA(dst, b, h) do { _Pragma("unroll") for (int m = 0; m < 4; ++m) _Pragma("unroll") for (int k = 0; k < 2; ++k) dst[m][k] = *(const LAS bf16x8*)(lds + PG8_SA(b, h) + aoff + m * 2048 + k * 1024); } while (0)
; #define PG8_LDB(dst, b, h) do { _Pragma("unroll") for (int n = 0; n < 2; ++n) _Pragma("unroll") for (int k = 0; k < 2; ++k) dst[n][k] = *(const LAS bf16x8*)(lds + PG8_SB(b, h) + boff + n * 2048 + k * 1024); } while (0)
; #define PG8_WAIT_V(n) asm volatile("s_waitcnt vmcnt(" #n ")" ::: "memory")
; #define PG8_WAIT_L(n) asm volatile("s_waitcnt lgkmcnt(" #n ")" ::: "memory")
; #define PG8_BAR __builtin_amdgcn_s_barrier()
; #define PG8_SCHED __builtin_amdgcn_sched_barrier(0)
;     ...
;             PG8_LDB(B0, 1, 0); PG8_LDB(B1, 1, 1); PG8_SCHED; PG8_LDA(At, 1, 0); PG8_STAGE(PG8_SA(0, 1), a2, va[1]);
;             PG8_WAIT_V(8); PG8_WAIT_L(0); PG8_BAR; PG8_MMA(0, 0, At, B0); PG8_MMA(0, 1, At, B1); PG8_BAR; PG8_SCHED;
;             PG8_LDA(At, 1, 1); PG8_STAGE(PG8_SB(1, 0), b3, voffB); PG8_STAGE(PG8_SB(1, 1), b3 + hstep, voffB); PG8_STAGE(PG8_SA(1, 0), a3, va[0]);
;             PG8_WAIT_V(8); PG8_WAIT_L(0); PG8_BAR; PG8_MMA(1, 0, At, B0); PG8_MMA(1, 1, At, B1); PG8_BAR; PG8_SCHED;
;         }
.Lmy_z91_back:
	s_setprio 0
	s_barrier
	s_add_i32 s63, 0, 0x18000
	s_add_i32 s64, 0, 0x1c000
	v_add_u32_e32 v14, s63, v219
	v_add_u32_e32 v30, s64, v219
	ds_read_b128 v[2:5], v14
	ds_read_b128 v[6:9], v14 offset:1024
	ds_read_b128 v[10:13], v14 offset:2048
	ds_read_b128 v[14:17], v14 offset:3072
	ds_read_b128 v[18:21], v30
	ds_read_b128 v[22:25], v30 offset:1024
	ds_read_b128 v[26:29], v30 offset:2048
	ds_read_b128 v[30:33], v30 offset:3072
	s_mov_b32 m0, s43
	v_lshl_add_u64 v[214:215], s[38:39], 0, v[214:215]
	ds_read_b128 v[34:37], v225 offset:32768
	ds_read_b128 v[38:41], v225 offset:33792
	ds_read_b128 v[42:45], v225 offset:34816
	ds_read_b128 v[46:49], v225 offset:35840
	ds_read_b128 v[50:53], v225 offset:36864
	ds_read_b128 v[54:57], v225 offset:37888
	ds_read_b128 v[58:61], v225 offset:38912
	ds_read_b128 v[62:65], v225 offset:39936
	global_load_lds_dwordx4 v[214:215], off
	v_lshl_add_u64 v[212:213], s[38:39], 0, v[212:213]
	s_mov_b32 m0, s44
	s_nop 0
	global_load_lds_dwordx4 v[212:213], off
	s_waitcnt vmcnt(8)
	s_waitcnt lgkmcnt(0)
	s_barrier
	s_setprio 1
	s_waitcnt lgkmcnt(0)
	v_mfma_scale_f32_16x16x128_f8f6f4 v[190:193], v[2:9], v[34:41], v[190:193], v227, v226 op_sel_hi:[0,0,0]
	v_mfma_scale_f32_16x16x128_f8f6f4 v[186:189], v[10:17], v[34:41], v[186:189], v227, v226 op_sel_hi:[0,0,0]
	v_mfma_scale_f32_16x16x128_f8f6f4 v[182:185], v[2:9], v[42:49], v[182:185], v227, v226 op_sel_hi:[0,0,0]
	v_mfma_scale_f32_16x16x128_f8f6f4 v[178:181], v[10:17], v[42:49], v[178:181], v227, v226 op_sel_hi:[0,0,0]
	v_mfma_scale_f32_16x16x128_f8f6f4 v[158:161], v[2:9], v[50:57], v[158:161], v227, v226 op_sel_hi:[0,0,0]
	v_mfma_scale_f32_16x16x128_f8f6f4 v[154:157], v[10:17], v[50:57], v[154:157], v227, v226 op_sel_hi:[0,0,0]
	v_mfma_scale_f32_16x16x128_f8f6f4 v[150:153], v[2:9], v[58:65], v[150:153], v227, v226 op_sel_hi:[0,0,0]
	v_mfma_scale_f32_16x16x128_f8f6f4 v[146:149], v[10:17], v[58:65], v[146:149], v227, v226 op_sel_hi:[0,0,0]
	s_setprio 0
	s_setprio 1
	v_mfma_scale_f32_16x16x128_f8f6f4 v[174:177], v[18:25], v[34:41], v[174:177], v227, v226 op_sel_hi:[0,0,0]
	v_mfma_scale_f32_16x16x128_f8f6f4 v[170:173], v[26:33], v[34:41], v[170:173], v227, v226 op_sel_hi:[0,0,0]
	v_mfma_scale_f32_16x16x128_f8f6f4 v[166:169], v[18:25], v[42:49], v[166:169], v227, v226 op_sel_hi:[0,0,0]
	v_mfma_scale_f32_16x16x128_f8f6f4 v[162:165], v[26:33], v[42:49], v[162:165], v227, v226 op_sel_hi:[0,0,0]
	v_mfma_scale_f32_16x16x128_f8f6f4 v[142:145], v[18:25], v[50:57], v[142:145], v227, v226 op_sel_hi:[0,0,0]
	v_mfma_scale_f32_16x16x128_f8f6f4 v[138:141], v[26:33], v[50:57], v[138:141], v227, v226 op_sel_hi:[0,0,0]
	v_mfma_scale_f32_16x16x128_f8f6f4 v[134:137], v[18:25], v[58:65], v[134:137], v227, v226 op_sel_hi:[0,0,0]
	v_mfma_scale_f32_16x16x128_f8f6f4 v[130:133], v[26:33], v[58:65], v[130:133], v227, v226 op_sel_hi:[0,0,0]
	s_setprio 0
	s_barrier
	s_add_i32 s38, s63, s2
	v_lshl_add_u64 v[212:213], v[230:231], 0, s[10:11]
	s_mov_b32 m0, s38
	ds_read_b128 v[34:37], v225 offset:49152
	ds_read_b128 v[38:41], v225 offset:50176
	ds_read_b128 v[42:45], v225 offset:51200
	ds_read_b128 v[46:49], v225 offset:52224
	ds_read_b128 v[50:53], v225 offset:53248
	ds_read_b128 v[54:57], v225 offset:54272
	ds_read_b128 v[58:61], v225 offset:55296
	ds_read_b128 v[62:65], v225 offset:56320
	global_load_lds_dwordx4 v[212:213], off
	s_add_i32 m0, s38, 0x2000
	s_add_u32 s36, s36, 0x40080
	v_lshl_add_u64 v[212:213], v[232:233], 0, s[10:11]
	s_addc_u32 s37, s37, 0
	s_add_i32 s38, s64, s2
	global_load_lds_dwordx4 v[212:213], off
	v_lshl_add_u64 v[212:213], s[36:37], 0, v[198:199]
	s_mov_b32 m0, s38
	s_nop 0
	global_load_lds_dwordx4 v[212:213], off
	v_lshl_add_u64 v[212:213], s[36:37], 0, v[196:197]
	s_add_i32 m0, s38, 0x2000
	s_nop 0
	global_load_lds_dwordx4 v[212:213], off
	v_lshl_add_u64 v[212:213], v[234:235], 0, s[10:11]
	s_mov_b32 m0, s46
	s_nop 0
	global_load_lds_dwordx4 v[212:213], off
	v_lshl_add_u64 v[212:213], v[236:237], 0, s[10:11]
	s_mov_b32 m0, s47
	s_nop 0
	global_load_lds_dwordx4 v[212:213], off
	s_waitcnt vmcnt(8)
	s_waitcnt lgkmcnt(0)
	s_barrier
	s_setprio 1
	s_waitcnt lgkmcnt(0)
	v_mfma_scale_f32_16x16x128_f8f6f4 v[126:129], v[2:9], v[34:41], v[126:129], v227, v226 op_sel_hi:[0,0,0]
	v_mfma_scale_f32_16x16x128_f8f6f4 v[122:125], v[10:17], v[34:41], v[122:125], v227, v226 op_sel_hi:[0,0,0]
	v_mfma_scale_f32_16x16x128_f8f6f4 v[118:121], v[2:9], v[42:49], v[118:121], v227, v226 op_sel_hi:[0,0,0]
	v_mfma_scale_f32_16x16x128_f8f6f4 v[114:117], v[10:17], v[42:49], v[114:117], v227, v226 op_sel_hi:[0,0,0]
	v_mfma_scale_f32_16x16x128_f8f6f4 v[94:97], v[2:9], v[50:57], v[94:97], v227, v226 op_sel_hi:[0,0,0]
	v_mfma_scale_f32_16x16x128_f8f6f4 v[90:93], v[10:17], v[50:57], v[90:93], v227, v226 op_sel_hi:[0,0,0]
	v_mfma_scale_f32_16x16x128_f8f6f4 v[86:89], v[2:9], v[58:65], v[86:89], v227, v226 op_sel_hi:[0,0,0]
	v_mfma_scale_f32_16x16x128_f8f6f4 v[82:85], v[10:17], v[58:65], v[82:85], v227, v226 op_sel_hi:[0,0,0]
	s_setprio 0
	s_setprio 1
	v_mfma_scale_f32_16x16x128_f8f6f4 v[110:113], v[18:25], v[34:41], v[110:113], v227, v226 op_sel_hi:[0,0,0]
	v_mfma_scale_f32_16x16x128_f8f6f4 v[106:109], v[26:33], v[34:41], v[106:109], v227, v226 op_sel_hi:[0,0,0]
	v_mfma_scale_f32_16x16x128_f8f6f4 v[102:105], v[18:25], v[42:49], v[102:105], v227, v226 op_sel_hi:[0,0,0]
	v_mfma_scale_f32_16x16x128_f8f6f4 v[98:101], v[26:33], v[42:49], v[98:101], v227, v226 op_sel_hi:[0,0,0]
	v_mfma_scale_f32_16x16x128_f8f6f4 v[78:81], v[18:25], v[50:57], v[78:81], v227, v226 op_sel_hi:[0,0,0]
	v_mfma_scale_f32_16x16x128_f8f6f4 v[74:77], v[26:33], v[50:57], v[74:77], v227, v226 op_sel_hi:[0,0,0]
	v_mfma_scale_f32_16x16x128_f8f6f4 v[70:73], v[18:25], v[58:65], v[70:73], v227, v226 op_sel_hi:[0,0,0]
	v_mfma_scale_f32_16x16x128_f8f6f4 v[66:69], v[26:33], v[58:65], v[66:69], v227, v226 op_sel_hi:[0,0,0]
	s_setprio 0
	s_barrier
	s_add_i32 s62, s62, 2
	s_add_u32 s27, s27, 0x100
	s_addc_u32 s29, s29, 0
	s_add_u32 s34, s34, 0x100
	s_addc_u32 s35, s35, 0
	s_cmp_gt_u32 s62, 13
	s_cbranch_scc1 .LBB0_1190
